# rebalance: 57 tile pairs per early converting workgroup, 22.5 per late joiner (uses the late joiners' measured slack)
# baseline (speedup 1.0000x reference)
; #define PW_SYNC do { asm volatile("s_waitcnt lgkmcnt(0)" ::: "memory"); __builtin_amdgcn_s_barrier(); asm volatile("" ::: "memory"); } while (0)
; __device__ __forceinline__ void ph_weights(const Params& p, LAS unsigned char* lds, const int p0, const int p1, const int wi, const int wn) {
;     ...
;     int pi = p0 + wi; bool hA, hB;
;     PW_LOAD(pi, dA0, dA1, a0, a1, hA);
;     PW_LOAD(pi + wn, dB0, dB1, b0, b1, hB);
;     while (hA) {
;         { PW_TOLDS(dA0, a0, a1); PW_SYNC; const TDesc s0 = dA0, s1 = dA1; PW_LOAD(pi + 2 * wn, dA0, dA1, a0, a1, hA); PW_STORE(s0, s1); PW_SYNC; }
;         if (!hB) break;
;         { PW_TOLDS(dB0, b0, b1); PW_SYNC; const TDesc s0 = dB0, s1 = dB1; PW_LOAD(pi + 3 * wn, dB0, dB1, b0, b1, hB); PW_STORE(s0, s1); PW_SYNC; }
;         pi += 2 * wn;
;     }
; __global__ void __launch_bounds__(512, 2) mk_fwd(Params p) {
;     ...
;             } else { if (bx - MIX_GW < 4) ph_rbias(p, 0, bx - MIX_GW); ph_weights(p, lds, 240, 6880, bx - MIX_GW, G - MIX_GW); }
.LBB0_779:
	v_readlane_b32 s0, v249, 28
	s_nop 3
	s_cmpk_lt_u32 s0, 0xa0
	s_cbranch_scc1 .Lcv_late
	s_mul_i32 s0, s0, 1
	s_add_u32 s0, s0, 80
	s_movk_i32 s70, 95
	s_movk_i32 s73, 1
	s_movk_i32 s71, 0x1650
	s_mov_b32 s74, 0
	v_writelane_b32 v255, s29, 61
	s_branch .Lcv_common
.Lcv_late:
	v_readlane_b32 s0, v249, 28
	s_nop 3
	s_mul_i32 s0, s0, 1
	s_add_u32 s0, s0, 5584
	s_movk_i32 s70, 31
	s_movk_i32 s73, 1
	s_movk_i32 s71, 0x1920
	s_mov_b32 s74, 0
	v_writelane_b32 v255, s29, 61
	s_branch .Lcv_common
